# plus saddr-form DMA addresses in the four GEMM K-loops (44 VALU adds per iteration group removed) and the router bias loop's LDS reads batched
# baseline (speedup 1.0000x reference)
.LBB0_271:
	s_add_u32 s18, s16, 0xfffc0080
	s_addc_u32 s19, s17, -1
	s_add_i32 s44, 0, 0x10000
	s_cmp_eq_u32 s43, 12
	s_cselect_b32 s21, s11, s19
	s_cselect_b32 s20, s39, s18
	v_add_u32_e32 v143, s44, v137
	s_cselect_b32 s19, s9, s42
	s_cselect_b32 s18, s40, s41
	s_add_i32 s46, 0, 0x14000
	ds_read_b128 v[148:151], v143
	ds_read_b128 v[152:155], v143 offset:1024
	ds_read_b128 v[156:159], v143 offset:2048
	ds_read_b128 v[160:163], v143 offset:3072
	v_add_u32_e32 v143, s46, v137
	ds_read_b128 v[164:167], v143
	ds_read_b128 v[168:171], v143 offset:1024
	ds_read_b128 v[172:175], v143 offset:2048
	ds_read_b128 v[176:179], v143 offset:3072
	s_add_i32 m0, s28, 0xc000
	ds_read_b128 v[180:183], v141
	ds_read_b128 v[184:187], v141 offset:1024
	ds_read_b128 v[188:191], v141 offset:2048
	ds_read_b128 v[192:195], v141 offset:3072
	ds_read_b128 v[196:199], v141 offset:4096
	ds_read_b128 v[200:203], v141 offset:5120
	ds_read_b128 v[204:207], v141 offset:6144
	ds_read_b128 v[230:233], v141 offset:7168
	global_load_lds_dwordx4 v144, s[16:17]
	s_add_i32 m0, s28, 0xe000
	s_nop 0
	global_load_lds_dwordx4 v146, s[16:17]
	s_waitcnt vmcnt(8)
	s_waitcnt lgkmcnt(0)
	s_barrier
	s_setprio 1
	s_waitcnt lgkmcnt(0)
	v_mfma_f32_16x16x32_bf16 v[126:129], v[148:151], v[180:183], v[126:129]
	v_mfma_f32_16x16x32_bf16 v[122:125], v[156:159], v[180:183], v[122:125]
	v_mfma_f32_16x16x32_bf16 v[118:121], v[148:151], v[188:191], v[118:121]
	v_mfma_f32_16x16x32_bf16 v[110:113], v[156:159], v[188:191], v[110:113]
	v_mfma_f32_16x16x32_bf16 v[102:105], v[148:151], v[196:199], v[102:105]
	v_mfma_f32_16x16x32_bf16 v[98:101], v[156:159], v[196:199], v[98:101]
	v_mfma_f32_16x16x32_bf16 v[86:89], v[148:151], v[204:207], v[86:89]
	v_mfma_f32_16x16x32_bf16 v[78:81], v[156:159], v[204:207], v[78:81]
	v_mfma_f32_16x16x32_bf16 v[126:129], v[152:155], v[184:187], v[126:129]
	v_mfma_f32_16x16x32_bf16 v[122:125], v[160:163], v[184:187], v[122:125]
	v_mfma_f32_16x16x32_bf16 v[118:121], v[152:155], v[192:195], v[118:121]
	v_mfma_f32_16x16x32_bf16 v[110:113], v[160:163], v[192:195], v[110:113]
	v_mfma_f32_16x16x32_bf16 v[102:105], v[152:155], v[200:203], v[102:105]
	v_mfma_f32_16x16x32_bf16 v[98:101], v[160:163], v[200:203], v[98:101]
	v_mfma_f32_16x16x32_bf16 v[86:89], v[152:155], v[230:233], v[86:89]
	v_mfma_f32_16x16x32_bf16 v[78:81], v[160:163], v[230:233], v[78:81]
	s_setprio 0
	s_setprio 1
	v_mfma_f32_16x16x32_bf16 v[114:117], v[164:167], v[180:183], v[114:117]
	v_mfma_f32_16x16x32_bf16 v[106:109], v[172:175], v[180:183], v[106:109]
	v_mfma_f32_16x16x32_bf16 v[94:97], v[164:167], v[188:191], v[94:97]
	v_mfma_f32_16x16x32_bf16 v[90:93], v[172:175], v[188:191], v[90:93]
	v_mfma_f32_16x16x32_bf16 v[70:73], v[164:167], v[196:199], v[70:73]
	v_mfma_f32_16x16x32_bf16 v[66:69], v[172:175], v[196:199], v[66:69]
	v_mfma_f32_16x16x32_bf16 v[46:49], v[164:167], v[204:207], v[46:49]
	v_mfma_f32_16x16x32_bf16 v[42:45], v[172:175], v[204:207], v[42:45]
	v_mfma_f32_16x16x32_bf16 v[114:117], v[168:171], v[184:187], v[114:117]
	v_mfma_f32_16x16x32_bf16 v[106:109], v[176:179], v[184:187], v[106:109]
	v_mfma_f32_16x16x32_bf16 v[94:97], v[168:171], v[192:195], v[94:97]
	v_mfma_f32_16x16x32_bf16 v[90:93], v[176:179], v[192:195], v[90:93]
	v_mfma_f32_16x16x32_bf16 v[70:73], v[168:171], v[200:203], v[70:73]
	v_mfma_f32_16x16x32_bf16 v[66:69], v[176:179], v[200:203], v[66:69]
	v_mfma_f32_16x16x32_bf16 v[46:49], v[168:171], v[230:233], v[46:49]
	v_mfma_f32_16x16x32_bf16 v[42:45], v[176:179], v[230:233], v[42:45]
	s_setprio 0
	s_barrier
	s_add_i32 s44, s44, s27
	s_mov_b32 m0, s44
	ds_read_b128 v[180:183], v141 offset:16384
	ds_read_b128 v[184:187], v141 offset:17408
	ds_read_b128 v[188:191], v141 offset:18432
	ds_read_b128 v[192:195], v141 offset:19456
	ds_read_b128 v[196:199], v141 offset:20480
	ds_read_b128 v[200:203], v141 offset:21504
	ds_read_b128 v[204:207], v141 offset:22528
	ds_read_b128 v[230:233], v141 offset:23552
	global_load_lds_dwordx4 v134, s[18:19]
	s_add_i32 m0, s44, 0x2000
	s_add_u32 s44, s18, 0x40000
	s_addc_u32 s45, s19, 0
	s_add_i32 s46, s46, s27
	global_load_lds_dwordx4 v130, s[18:19]
	s_mov_b32 m0, s46
	v_lshl_add_u64 v[214:215], s[20:21], 0, v[132:133]
	global_load_lds_dwordx4 v134, s[44:45]
	s_add_i32 m0, s46, 0x2000
	s_nop 0
	global_load_lds_dwordx4 v130, s[44:45]
	v_lshl_add_u64 v[208:209], s[20:21], 0, v[0:1]
	s_mov_b32 m0, s28
	s_nop 0
	global_load_lds_dwordx4 v[208:209], off
	s_mov_b32 m0, s29
	s_nop 0
	global_load_lds_dwordx4 v[214:215], off
	s_waitcnt vmcnt(8)
	s_waitcnt lgkmcnt(0)
	s_barrier
	s_setprio 1
	s_waitcnt lgkmcnt(0)
	v_mfma_f32_16x16x32_bf16 v[30:33], v[148:151], v[180:183], v[30:33]
	v_mfma_f32_16x16x32_bf16 v[26:29], v[156:159], v[180:183], v[26:29]
	v_mfma_f32_16x16x32_bf16 v[22:25], v[148:151], v[188:191], v[22:25]
	v_mfma_f32_16x16x32_bf16 v[18:21], v[156:159], v[188:191], v[18:21]
	v_mfma_f32_16x16x32_bf16 v[14:17], v[148:151], v[196:199], v[14:17]
	v_mfma_f32_16x16x32_bf16 v[10:13], v[156:159], v[196:199], v[10:13]
	v_mfma_f32_16x16x32_bf16 v[6:9], v[148:151], v[204:207], v[6:9]
	v_mfma_f32_16x16x32_bf16 v[2:5], v[156:159], v[204:207], v[2:5]
	v_mfma_f32_16x16x32_bf16 v[30:33], v[152:155], v[184:187], v[30:33]
	v_mfma_f32_16x16x32_bf16 v[26:29], v[160:163], v[184:187], v[26:29]
	v_mfma_f32_16x16x32_bf16 v[22:25], v[152:155], v[192:195], v[22:25]
	v_mfma_f32_16x16x32_bf16 v[18:21], v[160:163], v[192:195], v[18:21]
	v_mfma_f32_16x16x32_bf16 v[14:17], v[152:155], v[200:203], v[14:17]
	v_mfma_f32_16x16x32_bf16 v[10:13], v[160:163], v[200:203], v[10:13]
	v_mfma_f32_16x16x32_bf16 v[6:9], v[152:155], v[230:233], v[6:9]
	v_mfma_f32_16x16x32_bf16 v[2:5], v[160:163], v[230:233], v[2:5]
	s_setprio 0
	s_setprio 1
	v_mfma_f32_16x16x32_bf16 v[74:77], v[164:167], v[180:183], v[74:77]
	v_mfma_f32_16x16x32_bf16 v[82:85], v[172:175], v[180:183], v[82:85]
	v_mfma_f32_16x16x32_bf16 v[58:61], v[164:167], v[188:191], v[58:61]
	v_mfma_f32_16x16x32_bf16 v[62:65], v[172:175], v[188:191], v[62:65]
	v_mfma_f32_16x16x32_bf16 v[50:53], v[164:167], v[196:199], v[50:53]
	v_mfma_f32_16x16x32_bf16 v[54:57], v[172:175], v[196:199], v[54:57]
	v_mfma_f32_16x16x32_bf16 v[34:37], v[164:167], v[204:207], v[34:37]
	v_mfma_f32_16x16x32_bf16 v[38:41], v[172:175], v[204:207], v[38:41]
	v_mfma_f32_16x16x32_bf16 v[74:77], v[168:171], v[184:187], v[74:77]
	v_mfma_f32_16x16x32_bf16 v[82:85], v[176:179], v[184:187], v[82:85]
	v_mfma_f32_16x16x32_bf16 v[58:61], v[168:171], v[192:195], v[58:61]
	v_mfma_f32_16x16x32_bf16 v[62:65], v[176:179], v[192:195], v[62:65]
	v_mfma_f32_16x16x32_bf16 v[50:53], v[168:171], v[200:203], v[50:53]
	v_mfma_f32_16x16x32_bf16 v[54:57], v[176:179], v[200:203], v[54:57]
	v_mfma_f32_16x16x32_bf16 v[34:37], v[168:171], v[230:233], v[34:37]
	v_mfma_f32_16x16x32_bf16 v[38:41], v[176:179], v[230:233], v[38:41]
	s_setprio 0
	s_barrier
	s_add_i32 s44, 0, 0x18000
	v_add_u32_e32 v143, s44, v137
	s_add_i32 s45, 0, 0x1c000
	ds_read_b128 v[148:151], v143
	ds_read_b128 v[152:155], v143 offset:1024
	ds_read_b128 v[156:159], v143 offset:2048
	ds_read_b128 v[160:163], v143 offset:3072
	v_add_u32_e32 v143, s45, v137
	ds_read_b128 v[164:167], v143
	ds_read_b128 v[168:171], v143 offset:1024
	ds_read_b128 v[172:175], v143 offset:2048
	ds_read_b128 v[176:179], v143 offset:3072
	s_add_u32 s20, s20, 0x40000
	s_addc_u32 s21, s21, 0
	s_mov_b32 m0, s30
	ds_read_b128 v[180:183], v141 offset:32768
	ds_read_b128 v[184:187], v141 offset:33792
	ds_read_b128 v[188:191], v141 offset:34816
	ds_read_b128 v[192:195], v141 offset:35840
	ds_read_b128 v[196:199], v141 offset:36864
	ds_read_b128 v[200:203], v141 offset:37888
	ds_read_b128 v[204:207], v141 offset:38912
	ds_read_b128 v[230:233], v141 offset:39936
	global_load_lds_dwordx4 v0, s[20:21]
	s_mov_b32 m0, s31
	s_nop 0
	global_load_lds_dwordx4 v132, s[20:21]
	s_waitcnt vmcnt(8)
	s_waitcnt lgkmcnt(0)
	s_barrier
	s_setprio 1
	s_waitcnt lgkmcnt(0)
	v_mfma_f32_16x16x32_bf16 v[126:129], v[148:151], v[180:183], v[126:129]
	v_mfma_f32_16x16x32_bf16 v[122:125], v[156:159], v[180:183], v[122:125]
	v_mfma_f32_16x16x32_bf16 v[118:121], v[148:151], v[188:191], v[118:121]
	v_mfma_f32_16x16x32_bf16 v[110:113], v[156:159], v[188:191], v[110:113]
	v_mfma_f32_16x16x32_bf16 v[102:105], v[148:151], v[196:199], v[102:105]
	v_mfma_f32_16x16x32_bf16 v[98:101], v[156:159], v[196:199], v[98:101]
	v_mfma_f32_16x16x32_bf16 v[86:89], v[148:151], v[204:207], v[86:89]
	v_mfma_f32_16x16x32_bf16 v[78:81], v[156:159], v[204:207], v[78:81]
	v_mfma_f32_16x16x32_bf16 v[126:129], v[152:155], v[184:187], v[126:129]
	v_mfma_f32_16x16x32_bf16 v[122:125], v[160:163], v[184:187], v[122:125]
	v_mfma_f32_16x16x32_bf16 v[118:121], v[152:155], v[192:195], v[118:121]
	v_mfma_f32_16x16x32_bf16 v[110:113], v[160:163], v[192:195], v[110:113]
	v_mfma_f32_16x16x32_bf16 v[102:105], v[152:155], v[200:203], v[102:105]
	v_mfma_f32_16x16x32_bf16 v[98:101], v[160:163], v[200:203], v[98:101]
	v_mfma_f32_16x16x32_bf16 v[86:89], v[152:155], v[230:233], v[86:89]
	v_mfma_f32_16x16x32_bf16 v[78:81], v[160:163], v[230:233], v[78:81]
	s_setprio 0
	s_setprio 1
	v_mfma_f32_16x16x32_bf16 v[114:117], v[164:167], v[180:183], v[114:117]
	v_mfma_f32_16x16x32_bf16 v[106:109], v[172:175], v[180:183], v[106:109]
	v_mfma_f32_16x16x32_bf16 v[94:97], v[164:167], v[188:191], v[94:97]
	v_mfma_f32_16x16x32_bf16 v[90:93], v[172:175], v[188:191], v[90:93]
	v_mfma_f32_16x16x32_bf16 v[70:73], v[164:167], v[196:199], v[70:73]
	v_mfma_f32_16x16x32_bf16 v[66:69], v[172:175], v[196:199], v[66:69]
	v_mfma_f32_16x16x32_bf16 v[46:49], v[164:167], v[204:207], v[46:49]
	v_mfma_f32_16x16x32_bf16 v[42:45], v[172:175], v[204:207], v[42:45]
	v_mfma_f32_16x16x32_bf16 v[114:117], v[168:171], v[184:187], v[114:117]
	v_mfma_f32_16x16x32_bf16 v[106:109], v[176:179], v[184:187], v[106:109]
	v_mfma_f32_16x16x32_bf16 v[94:97], v[168:171], v[192:195], v[94:97]
	v_mfma_f32_16x16x32_bf16 v[90:93], v[176:179], v[192:195], v[90:93]
	v_mfma_f32_16x16x32_bf16 v[70:73], v[168:171], v[200:203], v[70:73]
	v_mfma_f32_16x16x32_bf16 v[66:69], v[176:179], v[200:203], v[66:69]
	v_mfma_f32_16x16x32_bf16 v[46:49], v[168:171], v[230:233], v[46:49]
	v_mfma_f32_16x16x32_bf16 v[42:45], v[176:179], v[230:233], v[42:45]
	s_setprio 0
	s_barrier
	s_add_u32 s20, s18, 0x1000
	s_addc_u32 s21, s19, 0
	s_add_i32 s44, s44, s27
	s_mov_b32 m0, s44
	ds_read_b128 v[180:183], v141 offset:49152
	ds_read_b128 v[184:187], v141 offset:50176
	ds_read_b128 v[188:191], v141 offset:51200
	ds_read_b128 v[192:195], v141 offset:52224
	ds_read_b128 v[196:199], v141 offset:53248
	ds_read_b128 v[200:203], v141 offset:54272
	ds_read_b128 v[204:207], v141 offset:55296
	ds_read_b128 v[230:233], v141 offset:56320
	global_load_lds_dwordx4 v134, s[20:21]
	s_add_i32 m0, s44, 0x2000
	s_add_u32 s18, s18, 0x41000
	v_lshl_add_u64 v[234:235], s[20:21], 0, v[130:131]
	s_addc_u32 s19, s19, 0
	s_add_i32 s20, s45, s27
	global_load_lds_dwordx4 v[234:235], off
	s_mov_b32 m0, s20
	v_lshl_add_u64 v[208:209], v[208:209], 0, s[48:49]
	global_load_lds_dwordx4 v134, s[18:19]
	s_add_i32 m0, s20, 0x2000
	s_nop 0
	global_load_lds_dwordx4 v130, s[18:19]
	s_mov_b32 m0, s34
	s_nop 0
	global_load_lds_dwordx4 v[208:209], off
	v_lshl_add_u64 v[208:209], v[214:215], 0, s[48:49]
	s_mov_b32 m0, s35
	s_nop 0
	global_load_lds_dwordx4 v[208:209], off
	s_waitcnt vmcnt(8)
	s_waitcnt lgkmcnt(0)
	s_barrier
	s_setprio 1
	s_waitcnt lgkmcnt(0)
	v_mfma_f32_16x16x32_bf16 v[30:33], v[148:151], v[180:183], v[30:33]
	v_mfma_f32_16x16x32_bf16 v[26:29], v[156:159], v[180:183], v[26:29]
	v_mfma_f32_16x16x32_bf16 v[22:25], v[148:151], v[188:191], v[22:25]
	v_mfma_f32_16x16x32_bf16 v[18:21], v[156:159], v[188:191], v[18:21]
	v_mfma_f32_16x16x32_bf16 v[14:17], v[148:151], v[196:199], v[14:17]
	v_mfma_f32_16x16x32_bf16 v[10:13], v[156:159], v[196:199], v[10:13]
	v_mfma_f32_16x16x32_bf16 v[6:9], v[148:151], v[204:207], v[6:9]
	v_mfma_f32_16x16x32_bf16 v[2:5], v[156:159], v[204:207], v[2:5]
	v_mfma_f32_16x16x32_bf16 v[30:33], v[152:155], v[184:187], v[30:33]
	v_mfma_f32_16x16x32_bf16 v[26:29], v[160:163], v[184:187], v[26:29]
	v_mfma_f32_16x16x32_bf16 v[22:25], v[152:155], v[192:195], v[22:25]
	v_mfma_f32_16x16x32_bf16 v[18:21], v[160:163], v[192:195], v[18:21]
	v_mfma_f32_16x16x32_bf16 v[14:17], v[152:155], v[200:203], v[14:17]
	v_mfma_f32_16x16x32_bf16 v[10:13], v[160:163], v[200:203], v[10:13]
	v_mfma_f32_16x16x32_bf16 v[6:9], v[152:155], v[230:233], v[6:9]
	v_mfma_f32_16x16x32_bf16 v[2:5], v[160:163], v[230:233], v[2:5]
	s_setprio 0
	s_setprio 1
	v_mfma_f32_16x16x32_bf16 v[74:77], v[164:167], v[180:183], v[74:77]
	v_mfma_f32_16x16x32_bf16 v[82:85], v[172:175], v[180:183], v[82:85]
	v_mfma_f32_16x16x32_bf16 v[58:61], v[164:167], v[188:191], v[58:61]
	v_mfma_f32_16x16x32_bf16 v[62:65], v[172:175], v[188:191], v[62:65]
	v_mfma_f32_16x16x32_bf16 v[50:53], v[164:167], v[196:199], v[50:53]
	v_mfma_f32_16x16x32_bf16 v[54:57], v[172:175], v[196:199], v[54:57]
	v_mfma_f32_16x16x32_bf16 v[34:37], v[164:167], v[204:207], v[34:37]
	v_mfma_f32_16x16x32_bf16 v[38:41], v[172:175], v[204:207], v[38:41]
	v_mfma_f32_16x16x32_bf16 v[74:77], v[168:171], v[184:187], v[74:77]
	v_mfma_f32_16x16x32_bf16 v[82:85], v[176:179], v[184:187], v[82:85]
	v_mfma_f32_16x16x32_bf16 v[58:61], v[168:171], v[192:195], v[58:61]
	v_mfma_f32_16x16x32_bf16 v[62:65], v[176:179], v[192:195], v[62:65]
	v_mfma_f32_16x16x32_bf16 v[50:53], v[168:171], v[200:203], v[50:53]
	v_mfma_f32_16x16x32_bf16 v[54:57], v[176:179], v[200:203], v[54:57]
	v_mfma_f32_16x16x32_bf16 v[34:37], v[168:171], v[230:233], v[34:37]
	v_mfma_f32_16x16x32_bf16 v[38:41], v[176:179], v[230:233], v[38:41]
	s_setprio 0
	s_barrier
	s_add_i32 s43, s43, 2
	s_add_u32 s41, s41, 0x2000
	s_addc_u32 s42, s42, 0
	s_add_u32 s16, s16, 0x100
	s_addc_u32 s17, s17, 0
	s_cmp_gt_u32 s43, 13
	s_cbranch_scc0 .LBB0_271
	s_and_b64 vcc, exec, s[6:7]
	s_cbranch_vccz .LBB0_274
	s_barrier

.LBB0_1098:
	s_add_u32 s22, s20, 0xfffc0080
	s_addc_u32 s23, s21, -1
	s_add_i32 s52, 0, 0x10000
	s_cmp_eq_u32 s51, 12
	s_cselect_b32 s27, s11, s23
	s_cselect_b32 s26, s47, s22
	s_cselect_b32 s23, s9, s50
	s_cselect_b32 s22, s48, s49
	s_add_i32 s54, 0, 0x14000
	v_add_u32_e32 v142, s52, v163
	v_add_u32_e32 v160, s54, v163
	ds_read_b128 v[130:133], v142
	ds_read_b128 v[134:137], v142 offset:1024
	ds_read_b128 v[138:141], v142 offset:2048
	ds_read_b128 v[142:145], v142 offset:3072
	ds_read_b128 v[156:159], v160
	ds_read_b128 v[166:169], v160 offset:1024
	ds_read_b128 v[170:173], v160 offset:2048
	ds_read_b128 v[174:177], v160 offset:3072
	s_add_i32 m0, s17, 0xc000
	ds_read_b128 v[178:181], v165
	ds_read_b128 v[182:185], v165 offset:1024
	ds_read_b128 v[186:189], v165 offset:2048
	ds_read_b128 v[190:193], v165 offset:3072
	ds_read_b128 v[194:197], v165 offset:4096
	ds_read_b128 v[198:201], v165 offset:5120
	ds_read_b128 v[202:205], v165 offset:6144
	ds_read_b128 v[206:209], v165 offset:7168
	global_load_lds_dwordx4 v152, s[20:21]
	s_add_i32 m0, s17, 0xe000
	s_nop 0
	global_load_lds_dwordx4 v154, s[20:21]
	s_waitcnt vmcnt(8)
	s_waitcnt lgkmcnt(0)
	s_barrier
	s_setprio 1
	s_waitcnt lgkmcnt(0)
	v_mfma_f32_16x16x32_bf16 v[126:129], v[130:133], v[178:181], v[126:129]
	v_mfma_f32_16x16x32_bf16 v[122:125], v[138:141], v[178:181], v[122:125]
	v_mfma_f32_16x16x32_bf16 v[118:121], v[130:133], v[186:189], v[118:121]
	v_mfma_f32_16x16x32_bf16 v[110:113], v[138:141], v[186:189], v[110:113]
	v_mfma_f32_16x16x32_bf16 v[102:105], v[130:133], v[194:197], v[102:105]
	v_mfma_f32_16x16x32_bf16 v[94:97], v[138:141], v[194:197], v[94:97]
	v_mfma_f32_16x16x32_bf16 v[86:89], v[130:133], v[202:205], v[86:89]
	v_mfma_f32_16x16x32_bf16 v[78:81], v[138:141], v[202:205], v[78:81]
	v_mfma_f32_16x16x32_bf16 v[126:129], v[134:137], v[182:185], v[126:129]
	v_mfma_f32_16x16x32_bf16 v[122:125], v[142:145], v[182:185], v[122:125]
	v_mfma_f32_16x16x32_bf16 v[118:121], v[134:137], v[190:193], v[118:121]
	v_mfma_f32_16x16x32_bf16 v[110:113], v[142:145], v[190:193], v[110:113]
	v_mfma_f32_16x16x32_bf16 v[102:105], v[134:137], v[198:201], v[102:105]
	v_mfma_f32_16x16x32_bf16 v[94:97], v[142:145], v[198:201], v[94:97]
	v_mfma_f32_16x16x32_bf16 v[86:89], v[134:137], v[206:209], v[86:89]
	v_mfma_f32_16x16x32_bf16 v[78:81], v[142:145], v[206:209], v[78:81]
	s_setprio 0
	s_setprio 1
	v_mfma_f32_16x16x32_bf16 v[114:117], v[156:159], v[178:181], v[114:117]
	v_mfma_f32_16x16x32_bf16 v[106:109], v[170:173], v[178:181], v[106:109]
	v_mfma_f32_16x16x32_bf16 v[98:101], v[156:159], v[186:189], v[98:101]
	v_mfma_f32_16x16x32_bf16 v[90:93], v[170:173], v[186:189], v[90:93]
	v_mfma_f32_16x16x32_bf16 v[82:85], v[156:159], v[194:197], v[82:85]
	v_mfma_f32_16x16x32_bf16 v[74:77], v[170:173], v[194:197], v[74:77]
	v_mfma_f32_16x16x32_bf16 v[70:73], v[156:159], v[202:205], v[70:73]
	v_mfma_f32_16x16x32_bf16 v[62:65], v[170:173], v[202:205], v[62:65]
	v_mfma_f32_16x16x32_bf16 v[114:117], v[166:169], v[182:185], v[114:117]
	v_mfma_f32_16x16x32_bf16 v[106:109], v[174:177], v[182:185], v[106:109]
	v_mfma_f32_16x16x32_bf16 v[98:101], v[166:169], v[190:193], v[98:101]
	v_mfma_f32_16x16x32_bf16 v[90:93], v[174:177], v[190:193], v[90:93]
	v_mfma_f32_16x16x32_bf16 v[82:85], v[166:169], v[198:201], v[82:85]
	v_mfma_f32_16x16x32_bf16 v[74:77], v[174:177], v[198:201], v[74:77]
	v_mfma_f32_16x16x32_bf16 v[70:73], v[166:169], v[206:209], v[70:73]
	v_mfma_f32_16x16x32_bf16 v[62:65], v[174:177], v[206:209], v[62:65]
	s_setprio 0
	s_barrier
	s_add_i32 s52, s52, s33
	s_mov_b32 m0, s52
	ds_read_b128 v[178:181], v165 offset:16384
	ds_read_b128 v[182:185], v165 offset:17408
	ds_read_b128 v[186:189], v165 offset:18432
	ds_read_b128 v[190:193], v165 offset:19456
	ds_read_b128 v[194:197], v165 offset:20480
	ds_read_b128 v[198:201], v165 offset:21504
	ds_read_b128 v[202:205], v165 offset:22528
	ds_read_b128 v[206:209], v165 offset:23552
	global_load_lds_dwordx4 v150, s[22:23]
	s_add_i32 m0, s52, 0x2000
	s_add_u32 s52, s22, 0x40000
	s_addc_u32 s53, s23, 0
	s_add_i32 s54, s54, s33
	global_load_lds_dwordx4 v146, s[22:23]
	s_mov_b32 m0, s54
	v_lshl_add_u64 v[210:211], s[26:27], 0, v[148:149]
	global_load_lds_dwordx4 v150, s[52:53]
	s_add_i32 m0, s54, 0x2000
	s_nop 0
	global_load_lds_dwordx4 v146, s[52:53]
	v_lshl_add_u64 v[160:161], s[26:27], 0, v[0:1]
	s_mov_b32 m0, s17
	s_nop 0
	global_load_lds_dwordx4 v[160:161], off
	s_mov_b32 m0, s19
	s_nop 0
	global_load_lds_dwordx4 v[210:211], off
	s_waitcnt vmcnt(8)
	s_waitcnt lgkmcnt(0)
	s_barrier
	s_setprio 1
	s_waitcnt lgkmcnt(0)
	v_mfma_f32_16x16x32_bf16 v[50:53], v[130:133], v[178:181], v[50:53]
	v_mfma_f32_16x16x32_bf16 v[42:45], v[138:141], v[178:181], v[42:45]
	v_mfma_f32_16x16x32_bf16 v[30:33], v[130:133], v[186:189], v[30:33]
	v_mfma_f32_16x16x32_bf16 v[22:25], v[138:141], v[186:189], v[22:25]
	v_mfma_f32_16x16x32_bf16 v[14:17], v[130:133], v[194:197], v[14:17]
	v_mfma_f32_16x16x32_bf16 v[10:13], v[138:141], v[194:197], v[10:13]
	v_mfma_f32_16x16x32_bf16 v[6:9], v[130:133], v[202:205], v[6:9]
	v_mfma_f32_16x16x32_bf16 v[2:5], v[138:141], v[202:205], v[2:5]
	v_mfma_f32_16x16x32_bf16 v[50:53], v[134:137], v[182:185], v[50:53]
	v_mfma_f32_16x16x32_bf16 v[42:45], v[142:145], v[182:185], v[42:45]
	v_mfma_f32_16x16x32_bf16 v[30:33], v[134:137], v[190:193], v[30:33]
	v_mfma_f32_16x16x32_bf16 v[22:25], v[142:145], v[190:193], v[22:25]
	v_mfma_f32_16x16x32_bf16 v[14:17], v[134:137], v[198:201], v[14:17]
	v_mfma_f32_16x16x32_bf16 v[10:13], v[142:145], v[198:201], v[10:13]
	v_mfma_f32_16x16x32_bf16 v[6:9], v[134:137], v[206:209], v[6:9]
	v_mfma_f32_16x16x32_bf16 v[2:5], v[142:145], v[206:209], v[2:5]
	s_setprio 0
	s_setprio 1
	v_mfma_f32_16x16x32_bf16 v[66:69], v[156:159], v[178:181], v[66:69]
	v_mfma_f32_16x16x32_bf16 v[58:61], v[170:173], v[178:181], v[58:61]
	v_mfma_f32_16x16x32_bf16 v[54:57], v[156:159], v[186:189], v[54:57]
	v_mfma_f32_16x16x32_bf16 v[46:49], v[170:173], v[186:189], v[46:49]
	v_mfma_f32_16x16x32_bf16 v[38:41], v[156:159], v[194:197], v[38:41]
	v_mfma_f32_16x16x32_bf16 v[34:37], v[170:173], v[194:197], v[34:37]
	v_mfma_f32_16x16x32_bf16 v[26:29], v[156:159], v[202:205], v[26:29]
	v_mfma_f32_16x16x32_bf16 v[18:21], v[170:173], v[202:205], v[18:21]
	v_mfma_f32_16x16x32_bf16 v[66:69], v[166:169], v[182:185], v[66:69]
	v_mfma_f32_16x16x32_bf16 v[58:61], v[174:177], v[182:185], v[58:61]
	v_mfma_f32_16x16x32_bf16 v[54:57], v[166:169], v[190:193], v[54:57]
	v_mfma_f32_16x16x32_bf16 v[46:49], v[174:177], v[190:193], v[46:49]
	v_mfma_f32_16x16x32_bf16 v[38:41], v[166:169], v[198:201], v[38:41]
	v_mfma_f32_16x16x32_bf16 v[34:37], v[174:177], v[198:201], v[34:37]
	v_mfma_f32_16x16x32_bf16 v[26:29], v[166:169], v[206:209], v[26:29]
	v_mfma_f32_16x16x32_bf16 v[18:21], v[174:177], v[206:209], v[18:21]
	s_setprio 0
	s_barrier
	s_add_i32 s52, 0, 0x18000
	s_add_i32 s53, 0, 0x1c000
	v_add_u32_e32 v142, s52, v163
	v_add_u32_e32 v174, s53, v163
	ds_read_b128 v[130:133], v142
	ds_read_b128 v[134:137], v142 offset:1024
	ds_read_b128 v[138:141], v142 offset:2048
	ds_read_b128 v[142:145], v142 offset:3072
	ds_read_b128 v[156:159], v174
	ds_read_b128 v[166:169], v174 offset:1024
	ds_read_b128 v[170:173], v174 offset:2048
	ds_read_b128 v[174:177], v174 offset:3072
	s_add_u32 s26, s26, 0x40000
	s_addc_u32 s27, s27, 0
	s_mov_b32 m0, s36
	ds_read_b128 v[178:181], v165 offset:32768
	ds_read_b128 v[182:185], v165 offset:33792
	ds_read_b128 v[186:189], v165 offset:34816
	ds_read_b128 v[190:193], v165 offset:35840
	ds_read_b128 v[194:197], v165 offset:36864
	ds_read_b128 v[198:201], v165 offset:37888
	ds_read_b128 v[202:205], v165 offset:38912
	ds_read_b128 v[206:209], v165 offset:39936
	global_load_lds_dwordx4 v0, s[26:27]
	s_mov_b32 m0, s37
	s_nop 0
	global_load_lds_dwordx4 v148, s[26:27]
	s_waitcnt vmcnt(8)
	s_waitcnt lgkmcnt(0)
	s_barrier
	s_setprio 1
	s_waitcnt lgkmcnt(0)
	v_mfma_f32_16x16x32_bf16 v[126:129], v[130:133], v[178:181], v[126:129]
	v_mfma_f32_16x16x32_bf16 v[122:125], v[138:141], v[178:181], v[122:125]
	v_mfma_f32_16x16x32_bf16 v[118:121], v[130:133], v[186:189], v[118:121]
	v_mfma_f32_16x16x32_bf16 v[110:113], v[138:141], v[186:189], v[110:113]
	v_mfma_f32_16x16x32_bf16 v[102:105], v[130:133], v[194:197], v[102:105]
	v_mfma_f32_16x16x32_bf16 v[94:97], v[138:141], v[194:197], v[94:97]
	v_mfma_f32_16x16x32_bf16 v[86:89], v[130:133], v[202:205], v[86:89]
	v_mfma_f32_16x16x32_bf16 v[78:81], v[138:141], v[202:205], v[78:81]
	v_mfma_f32_16x16x32_bf16 v[126:129], v[134:137], v[182:185], v[126:129]
	v_mfma_f32_16x16x32_bf16 v[122:125], v[142:145], v[182:185], v[122:125]
	v_mfma_f32_16x16x32_bf16 v[118:121], v[134:137], v[190:193], v[118:121]
	v_mfma_f32_16x16x32_bf16 v[110:113], v[142:145], v[190:193], v[110:113]
	v_mfma_f32_16x16x32_bf16 v[102:105], v[134:137], v[198:201], v[102:105]
	v_mfma_f32_16x16x32_bf16 v[94:97], v[142:145], v[198:201], v[94:97]
	v_mfma_f32_16x16x32_bf16 v[86:89], v[134:137], v[206:209], v[86:89]
	v_mfma_f32_16x16x32_bf16 v[78:81], v[142:145], v[206:209], v[78:81]
	s_setprio 0
	s_setprio 1
	v_mfma_f32_16x16x32_bf16 v[114:117], v[156:159], v[178:181], v[114:117]
	v_mfma_f32_16x16x32_bf16 v[106:109], v[170:173], v[178:181], v[106:109]
	v_mfma_f32_16x16x32_bf16 v[98:101], v[156:159], v[186:189], v[98:101]
	v_mfma_f32_16x16x32_bf16 v[90:93], v[170:173], v[186:189], v[90:93]
	v_mfma_f32_16x16x32_bf16 v[82:85], v[156:159], v[194:197], v[82:85]
	v_mfma_f32_16x16x32_bf16 v[74:77], v[170:173], v[194:197], v[74:77]
	v_mfma_f32_16x16x32_bf16 v[70:73], v[156:159], v[202:205], v[70:73]
	v_mfma_f32_16x16x32_bf16 v[62:65], v[170:173], v[202:205], v[62:65]
	v_mfma_f32_16x16x32_bf16 v[114:117], v[166:169], v[182:185], v[114:117]
	v_mfma_f32_16x16x32_bf16 v[106:109], v[174:177], v[182:185], v[106:109]
	v_mfma_f32_16x16x32_bf16 v[98:101], v[166:169], v[190:193], v[98:101]
	v_mfma_f32_16x16x32_bf16 v[90:93], v[174:177], v[190:193], v[90:93]
	v_mfma_f32_16x16x32_bf16 v[82:85], v[166:169], v[198:201], v[82:85]
	v_mfma_f32_16x16x32_bf16 v[74:77], v[174:177], v[198:201], v[74:77]
	v_mfma_f32_16x16x32_bf16 v[70:73], v[166:169], v[206:209], v[70:73]
	v_mfma_f32_16x16x32_bf16 v[62:65], v[174:177], v[206:209], v[62:65]
	s_setprio 0
	s_barrier
	s_add_u32 s26, s22, 0x1000
	s_addc_u32 s27, s23, 0
	s_add_i32 s52, s52, s33
	s_mov_b32 m0, s52
	ds_read_b128 v[178:181], v165 offset:49152
	ds_read_b128 v[182:185], v165 offset:50176
	ds_read_b128 v[186:189], v165 offset:51200
	ds_read_b128 v[190:193], v165 offset:52224
	ds_read_b128 v[194:197], v165 offset:53248
	ds_read_b128 v[198:201], v165 offset:54272
	ds_read_b128 v[202:205], v165 offset:55296
	ds_read_b128 v[206:209], v165 offset:56320
	global_load_lds_dwordx4 v150, s[26:27]
	s_add_i32 m0, s52, 0x2000
	s_add_u32 s22, s22, 0x41000
	v_lshl_add_u64 v[212:213], s[26:27], 0, v[146:147]
	s_addc_u32 s23, s23, 0
	s_add_i32 s26, s53, s33
	global_load_lds_dwordx4 v[212:213], off
	s_mov_b32 m0, s26
	v_lshl_add_u64 v[160:161], v[160:161], 0, s[56:57]
	global_load_lds_dwordx4 v150, s[22:23]
	s_add_i32 m0, s26, 0x2000
	s_nop 0
	global_load_lds_dwordx4 v146, s[22:23]
	s_mov_b32 m0, s42
	s_nop 0
	global_load_lds_dwordx4 v[160:161], off
	v_lshl_add_u64 v[160:161], v[210:211], 0, s[56:57]
	s_mov_b32 m0, s43
	s_nop 0
	global_load_lds_dwordx4 v[160:161], off
	s_waitcnt vmcnt(8)
	s_waitcnt lgkmcnt(0)
	s_barrier
	s_setprio 1
	s_waitcnt lgkmcnt(0)
	v_mfma_f32_16x16x32_bf16 v[50:53], v[130:133], v[178:181], v[50:53]
	v_mfma_f32_16x16x32_bf16 v[42:45], v[138:141], v[178:181], v[42:45]
	v_mfma_f32_16x16x32_bf16 v[30:33], v[130:133], v[186:189], v[30:33]
	v_mfma_f32_16x16x32_bf16 v[22:25], v[138:141], v[186:189], v[22:25]
	v_mfma_f32_16x16x32_bf16 v[14:17], v[130:133], v[194:197], v[14:17]
	v_mfma_f32_16x16x32_bf16 v[10:13], v[138:141], v[194:197], v[10:13]
	v_mfma_f32_16x16x32_bf16 v[6:9], v[130:133], v[202:205], v[6:9]
	v_mfma_f32_16x16x32_bf16 v[2:5], v[138:141], v[202:205], v[2:5]
	v_mfma_f32_16x16x32_bf16 v[50:53], v[134:137], v[182:185], v[50:53]
	v_mfma_f32_16x16x32_bf16 v[42:45], v[142:145], v[182:185], v[42:45]
	v_mfma_f32_16x16x32_bf16 v[30:33], v[134:137], v[190:193], v[30:33]
	v_mfma_f32_16x16x32_bf16 v[22:25], v[142:145], v[190:193], v[22:25]
	v_mfma_f32_16x16x32_bf16 v[14:17], v[134:137], v[198:201], v[14:17]
	v_mfma_f32_16x16x32_bf16 v[10:13], v[142:145], v[198:201], v[10:13]
	v_mfma_f32_16x16x32_bf16 v[6:9], v[134:137], v[206:209], v[6:9]
	v_mfma_f32_16x16x32_bf16 v[2:5], v[142:145], v[206:209], v[2:5]
	s_setprio 0
	s_setprio 1
	v_mfma_f32_16x16x32_bf16 v[66:69], v[156:159], v[178:181], v[66:69]
	v_mfma_f32_16x16x32_bf16 v[58:61], v[170:173], v[178:181], v[58:61]
	v_mfma_f32_16x16x32_bf16 v[54:57], v[156:159], v[186:189], v[54:57]
	v_mfma_f32_16x16x32_bf16 v[46:49], v[170:173], v[186:189], v[46:49]
	v_mfma_f32_16x16x32_bf16 v[38:41], v[156:159], v[194:197], v[38:41]
	v_mfma_f32_16x16x32_bf16 v[34:37], v[170:173], v[194:197], v[34:37]
	v_mfma_f32_16x16x32_bf16 v[26:29], v[156:159], v[202:205], v[26:29]
	v_mfma_f32_16x16x32_bf16 v[18:21], v[170:173], v[202:205], v[18:21]
	v_mfma_f32_16x16x32_bf16 v[66:69], v[166:169], v[182:185], v[66:69]
	v_mfma_f32_16x16x32_bf16 v[58:61], v[174:177], v[182:185], v[58:61]
	v_mfma_f32_16x16x32_bf16 v[54:57], v[166:169], v[190:193], v[54:57]
	v_mfma_f32_16x16x32_bf16 v[46:49], v[174:177], v[190:193], v[46:49]
	v_mfma_f32_16x16x32_bf16 v[38:41], v[166:169], v[198:201], v[38:41]
	v_mfma_f32_16x16x32_bf16 v[34:37], v[174:177], v[198:201], v[34:37]
	v_mfma_f32_16x16x32_bf16 v[26:29], v[166:169], v[206:209], v[26:29]
	v_mfma_f32_16x16x32_bf16 v[18:21], v[174:177], v[206:209], v[18:21]
	s_setprio 0
	s_barrier
	s_add_i32 s51, s51, 2
	s_add_u32 s49, s49, 0x2000
	s_addc_u32 s50, s50, 0
	s_add_u32 s20, s20, 0x100
	s_addc_u32 s21, s21, 0
	s_cmp_gt_u32 s51, 13
	s_cbranch_scc0 .LBB0_1098
	s_and_b64 vcc, exec, s[2:3]
	s_cbranch_vccz .LBB0_1101
	s_barrier

.LBB0_1165:
	v_add_u32_e32 v9, 0, v8
	v_add_u32_e32 v10, 0x13100, v9
	v_add_u32_e32 v19, 0, v4
	v_add_u32_e32 v9, 0x13110, v9
	ds_read_b128 v[10:13], v10
	ds_read_b128 v[14:17], v19
	ds_read_b128 v[140:143], v9
	ds_read_b32 v144, v19 offset:256
	ds_read_b32 v145, v7
	ds_read_b32 v146, v6
	ds_read_b32 v147, v5
	s_add_i32 s5, s5, -8
	v_add_u32_e32 v4, 0x200, v4
	v_add_u32_e32 v8, 32, v8
	v_add_u32_e32 v7, 0x200, v7
	v_add_u32_e32 v6, 0x200, v6
	v_add_u32_e32 v5, 0x200, v5
	s_cmp_eq_u32 s5, 0
	s_waitcnt lgkmcnt(5)
	v_fmac_f32_e32 v2, v10, v14
	v_fmac_f32_e32 v2, v11, v15
	v_fmac_f32_e32 v2, v12, v16
	v_fmac_f32_e32 v2, v13, v17
	s_waitcnt lgkmcnt(3)
	v_fmac_f32_e32 v2, v140, v144
	s_waitcnt lgkmcnt(2)
	v_fmac_f32_e32 v2, v141, v145
	s_waitcnt lgkmcnt(1)
	v_fmac_f32_e32 v2, v142, v146
	s_waitcnt lgkmcnt(0)
	v_fmac_f32_e32 v2, v143, v147
	s_cbranch_scc0 .LBB0_1165
	v_mbcnt_lo_u32_b32 v4, -1, 0
	v_mbcnt_hi_u32_b32 v4, -1, v4
	v_cmp_eq_u32_e32 vcc, 0, v3
	v_lshlrev_b32_e32 v4, 2, v4
	v_xor_b32_e32 v4, 4, v4
	ds_bpermute_b32 v4, v4, v2
	s_waitcnt lgkmcnt(0)
	v_add_f32_e32 v2, v2, v4
	v_mbcnt_lo_u32_b32 v4, -1, 0
	v_mbcnt_hi_u32_b32 v4, -1, v4
	s_nop 0
	v_lshlrev_b32_e32 v4, 2, v4
	v_xor_b32_e32 v4, 8, v4
	ds_bpermute_b32 v4, v4, v2
	s_waitcnt lgkmcnt(0)
	v_add_f32_e32 v2, v2, v4
	v_mbcnt_lo_u32_b32 v4, -1, 0
	v_mbcnt_hi_u32_b32 v4, -1, v4
	s_nop 0
	v_lshlrev_b32_e32 v4, 2, v4
	v_xor_b32_e32 v4, 16, v4
	ds_bpermute_b32 v4, v4, v2
	s_and_b64 exec, exec, vcc
	s_cbranch_execz .LBB0_1168
	v_lshl_add_u32 v0, v0, 2, 0
	s_waitcnt lgkmcnt(0)
	v_add_f32_e32 v2, v2, v4
	v_add_u32_e32 v0, 0x13000, v0
	ds_write_b32 v0, v2

.LBB0_1737:
	s_add_u32 s24, s2, s22
	s_addc_u32 s25, s3, s23
	s_add_u32 s26, s24, 0x21c00100
	s_addc_u32 s27, s25, 0
	s_add_i32 s45, 0, 0x10000
	s_cmpk_eq_i32 s22, 0x700
	s_cselect_b64 vcc, -1, 0
	s_and_b64 s[24:25], vcc, exec
	s_cselect_b32 s27, s7, s27
	s_cselect_b32 s26, s6, s26
	v_add_u32_e32 v145, s45, v141
	s_cselect_b32 s25, s5, s43
	s_cselect_b32 s24, s4, s19
	s_add_i32 s48, 0, 0x14000
	ds_read_b128 v[160:163], v145
	ds_read_b128 v[164:167], v145 offset:1024
	ds_read_b128 v[168:171], v145 offset:2048
	ds_read_b128 v[172:175], v145 offset:3072
	v_add_u32_e32 v145, s48, v141
	ds_read_b128 v[176:179], v145
	ds_read_b128 v[180:183], v145 offset:1024
	ds_read_b128 v[184:187], v145 offset:2048
	ds_read_b128 v[188:191], v145 offset:3072
	v_cndmask_b32_e32 v0, v140, v156, vcc
	v_cndmask_b32_e32 v208, v138, v157, vcc
	v_cndmask_b32_e32 v137, v142, v158, vcc
	v_cndmask_b32_e32 v143, v144, v159, vcc
	v_lshl_add_u64 v[210:211], v[148:149], 0, s[22:23]
	s_add_i32 m0, s33, 0xc000
	ds_read_b128 v[192:195], v155
	ds_read_b128 v[196:199], v155 offset:1024
	ds_read_b128 v[200:203], v155 offset:2048
	ds_read_b128 v[204:207], v155 offset:3072
	ds_read_b128 v[230:233], v155 offset:4096
	ds_read_b128 v[234:237], v155 offset:5120
	ds_read_b128 v[238:241], v155 offset:6144
	ds_read_b128 v[242:245], v155 offset:7168
	global_load_lds_dwordx4 v[210:211], off
	v_lshl_add_u64 v[210:211], v[146:147], 0, s[22:23]
	s_add_i32 m0, s33, 0xe000
	s_nop 0
	global_load_lds_dwordx4 v[210:211], off
	s_waitcnt vmcnt(8)
	s_waitcnt lgkmcnt(0)
	s_barrier
	s_setprio 1
	s_waitcnt lgkmcnt(0)
	v_mfma_f32_16x16x32_bf16 v[126:129], v[160:163], v[192:195], v[126:129]
	v_mfma_f32_16x16x32_bf16 v[122:125], v[168:171], v[192:195], v[122:125]
	v_mfma_f32_16x16x32_bf16 v[110:113], v[160:163], v[200:203], v[110:113]
	v_mfma_f32_16x16x32_bf16 v[106:109], v[168:171], v[200:203], v[106:109]
	v_mfma_f32_16x16x32_bf16 v[94:97], v[160:163], v[230:233], v[94:97]
	v_mfma_f32_16x16x32_bf16 v[90:93], v[168:171], v[230:233], v[90:93]
	v_mfma_f32_16x16x32_bf16 v[78:81], v[160:163], v[238:241], v[78:81]
	v_mfma_f32_16x16x32_bf16 v[74:77], v[168:171], v[238:241], v[74:77]
	v_mfma_f32_16x16x32_bf16 v[126:129], v[164:167], v[196:199], v[126:129]
	v_mfma_f32_16x16x32_bf16 v[122:125], v[172:175], v[196:199], v[122:125]
	v_mfma_f32_16x16x32_bf16 v[110:113], v[164:167], v[204:207], v[110:113]
	v_mfma_f32_16x16x32_bf16 v[106:109], v[172:175], v[204:207], v[106:109]
	v_mfma_f32_16x16x32_bf16 v[94:97], v[164:167], v[234:237], v[94:97]
	v_mfma_f32_16x16x32_bf16 v[90:93], v[172:175], v[234:237], v[90:93]
	v_mfma_f32_16x16x32_bf16 v[78:81], v[164:167], v[242:245], v[78:81]
	v_mfma_f32_16x16x32_bf16 v[74:77], v[172:175], v[242:245], v[74:77]
	s_setprio 0
	s_setprio 1
	v_mfma_f32_16x16x32_bf16 v[118:121], v[176:179], v[192:195], v[118:121]
	v_mfma_f32_16x16x32_bf16 v[114:117], v[184:187], v[192:195], v[114:117]
	v_mfma_f32_16x16x32_bf16 v[102:105], v[176:179], v[200:203], v[102:105]
	v_mfma_f32_16x16x32_bf16 v[98:101], v[184:187], v[200:203], v[98:101]
	v_mfma_f32_16x16x32_bf16 v[86:89], v[176:179], v[230:233], v[86:89]
	v_mfma_f32_16x16x32_bf16 v[82:85], v[184:187], v[230:233], v[82:85]
	v_mfma_f32_16x16x32_bf16 v[70:73], v[176:179], v[238:241], v[70:73]
	v_mfma_f32_16x16x32_bf16 v[66:69], v[184:187], v[238:241], v[66:69]
	v_mfma_f32_16x16x32_bf16 v[118:121], v[180:183], v[196:199], v[118:121]
	v_mfma_f32_16x16x32_bf16 v[114:117], v[188:191], v[196:199], v[114:117]
	v_mfma_f32_16x16x32_bf16 v[102:105], v[180:183], v[204:207], v[102:105]
	v_mfma_f32_16x16x32_bf16 v[98:101], v[188:191], v[204:207], v[98:101]
	v_mfma_f32_16x16x32_bf16 v[86:89], v[180:183], v[234:237], v[86:89]
	v_mfma_f32_16x16x32_bf16 v[82:85], v[188:191], v[234:237], v[82:85]
	v_mfma_f32_16x16x32_bf16 v[70:73], v[180:183], v[242:245], v[70:73]
	v_mfma_f32_16x16x32_bf16 v[66:69], v[188:191], v[242:245], v[66:69]
	s_setprio 0
	s_barrier
	s_add_i32 s45, s45, s31
	s_mov_b32 m0, s45
	ds_read_b128 v[192:195], v155 offset:16384
	ds_read_b128 v[196:199], v155 offset:17408
	ds_read_b128 v[200:203], v155 offset:18432
	ds_read_b128 v[204:207], v155 offset:19456
	ds_read_b128 v[230:233], v155 offset:20480
	ds_read_b128 v[234:237], v155 offset:21504
	ds_read_b128 v[238:241], v155 offset:22528
	ds_read_b128 v[242:245], v155 offset:23552
	global_load_lds_dwordx4 v130, s[24:25]
	s_add_i32 m0, s45, 0x2000
	s_add_u32 s46, s24, 0x40000
	s_addc_u32 s47, s25, 0
	s_add_i32 s45, s48, s31
	global_load_lds_dwordx4 v132, s[24:25]
	s_mov_b32 m0, s45
	v_mov_b32_e32 v209, v1
	global_load_lds_dwordx4 v130, s[46:47]
	s_add_i32 m0, s45, 0x2000
	s_nop 0
	global_load_lds_dwordx4 v132, s[46:47]
	s_mov_b32 m0, s33
	v_lshl_add_u64 v[210:211], s[26:27], 0, v[0:1]
	global_load_lds_dwordx4 v0, s[26:27]
	s_mov_b32 m0, s34
	s_nop 0
	global_load_lds_dwordx4 v208, s[26:27]
	s_waitcnt vmcnt(8)
	s_waitcnt lgkmcnt(0)
	v_lshl_add_u64 v[208:209], s[26:27], 0, v[208:209]
	s_barrier
	s_setprio 1
	s_waitcnt lgkmcnt(0)
	v_mfma_f32_16x16x32_bf16 v[62:65], v[160:163], v[192:195], v[62:65]
	v_mfma_f32_16x16x32_bf16 v[58:61], v[168:171], v[192:195], v[58:61]
	v_mfma_f32_16x16x32_bf16 v[46:49], v[160:163], v[200:203], v[46:49]
	v_mfma_f32_16x16x32_bf16 v[42:45], v[168:171], v[200:203], v[42:45]
	v_mfma_f32_16x16x32_bf16 v[22:25], v[160:163], v[230:233], v[22:25]
	v_mfma_f32_16x16x32_bf16 v[10:13], v[168:171], v[230:233], v[10:13]
	v_mfma_f32_16x16x32_bf16 v[6:9], v[160:163], v[238:241], v[6:9]
	v_mfma_f32_16x16x32_bf16 v[2:5], v[168:171], v[238:241], v[2:5]
	v_mfma_f32_16x16x32_bf16 v[62:65], v[164:167], v[196:199], v[62:65]
	v_mfma_f32_16x16x32_bf16 v[58:61], v[172:175], v[196:199], v[58:61]
	v_mfma_f32_16x16x32_bf16 v[46:49], v[164:167], v[204:207], v[46:49]
	v_mfma_f32_16x16x32_bf16 v[42:45], v[172:175], v[204:207], v[42:45]
	v_mfma_f32_16x16x32_bf16 v[22:25], v[164:167], v[234:237], v[22:25]
	v_mfma_f32_16x16x32_bf16 v[10:13], v[172:175], v[234:237], v[10:13]
	v_mfma_f32_16x16x32_bf16 v[6:9], v[164:167], v[242:245], v[6:9]
	v_mfma_f32_16x16x32_bf16 v[2:5], v[172:175], v[242:245], v[2:5]
	s_setprio 0
	s_setprio 1
	v_mfma_f32_16x16x32_bf16 v[54:57], v[176:179], v[192:195], v[54:57]
	v_mfma_f32_16x16x32_bf16 v[50:53], v[184:187], v[192:195], v[50:53]
	v_mfma_f32_16x16x32_bf16 v[30:33], v[176:179], v[200:203], v[30:33]
	v_mfma_f32_16x16x32_bf16 v[26:29], v[184:187], v[200:203], v[26:29]
	v_mfma_f32_16x16x32_bf16 v[38:41], v[176:179], v[230:233], v[38:41]
	v_mfma_f32_16x16x32_bf16 v[34:37], v[184:187], v[230:233], v[34:37]
	v_mfma_f32_16x16x32_bf16 v[18:21], v[176:179], v[238:241], v[18:21]
	v_mfma_f32_16x16x32_bf16 v[14:17], v[184:187], v[238:241], v[14:17]
	v_mfma_f32_16x16x32_bf16 v[54:57], v[180:183], v[196:199], v[54:57]
	v_mfma_f32_16x16x32_bf16 v[50:53], v[188:191], v[196:199], v[50:53]
	v_mfma_f32_16x16x32_bf16 v[30:33], v[180:183], v[204:207], v[30:33]
	v_mfma_f32_16x16x32_bf16 v[26:29], v[188:191], v[204:207], v[26:29]
	v_mfma_f32_16x16x32_bf16 v[38:41], v[180:183], v[234:237], v[38:41]
	v_mfma_f32_16x16x32_bf16 v[34:37], v[188:191], v[234:237], v[34:37]
	v_mfma_f32_16x16x32_bf16 v[18:21], v[180:183], v[242:245], v[18:21]
	v_mfma_f32_16x16x32_bf16 v[14:17], v[188:191], v[242:245], v[14:17]
	s_setprio 0
	s_barrier
	s_add_i32 s45, 0, 0x18000
	v_add_u32_e32 v0, s45, v141
	s_add_i32 s46, 0, 0x1c000
	ds_read_b128 v[160:163], v0
	ds_read_b128 v[164:167], v0 offset:1024
	ds_read_b128 v[168:171], v0 offset:2048
	ds_read_b128 v[172:175], v0 offset:3072
	v_add_u32_e32 v0, s46, v141
	ds_read_b128 v[176:179], v0
	ds_read_b128 v[180:183], v0 offset:1024
	ds_read_b128 v[184:187], v0 offset:2048
	ds_read_b128 v[188:191], v0 offset:3072
	s_mov_b32 m0, s35
	ds_read_b128 v[192:195], v155 offset:32768
	ds_read_b128 v[196:199], v155 offset:33792
	ds_read_b128 v[200:203], v155 offset:34816
	ds_read_b128 v[204:207], v155 offset:35840
	ds_read_b128 v[230:233], v155 offset:36864
	ds_read_b128 v[234:237], v155 offset:37888
	ds_read_b128 v[238:241], v155 offset:38912
	ds_read_b128 v[242:245], v155 offset:39936
	global_load_lds_dwordx4 v137, s[26:27]
	s_mov_b32 m0, s36
	s_nop 0
	global_load_lds_dwordx4 v143, s[26:27]
	s_waitcnt vmcnt(8)
	s_waitcnt lgkmcnt(0)
	s_barrier
	s_setprio 1
	s_waitcnt lgkmcnt(0)
	v_mfma_f32_16x16x32_bf16 v[126:129], v[160:163], v[192:195], v[126:129]
	v_mfma_f32_16x16x32_bf16 v[122:125], v[168:171], v[192:195], v[122:125]
	v_mfma_f32_16x16x32_bf16 v[110:113], v[160:163], v[200:203], v[110:113]
	v_mfma_f32_16x16x32_bf16 v[106:109], v[168:171], v[200:203], v[106:109]
	v_mfma_f32_16x16x32_bf16 v[94:97], v[160:163], v[230:233], v[94:97]
	v_mfma_f32_16x16x32_bf16 v[90:93], v[168:171], v[230:233], v[90:93]
	v_mfma_f32_16x16x32_bf16 v[78:81], v[160:163], v[238:241], v[78:81]
	v_mfma_f32_16x16x32_bf16 v[74:77], v[168:171], v[238:241], v[74:77]
	v_mfma_f32_16x16x32_bf16 v[126:129], v[164:167], v[196:199], v[126:129]
	v_mfma_f32_16x16x32_bf16 v[122:125], v[172:175], v[196:199], v[122:125]
	v_mfma_f32_16x16x32_bf16 v[110:113], v[164:167], v[204:207], v[110:113]
	v_mfma_f32_16x16x32_bf16 v[106:109], v[172:175], v[204:207], v[106:109]
	v_mfma_f32_16x16x32_bf16 v[94:97], v[164:167], v[234:237], v[94:97]
	v_mfma_f32_16x16x32_bf16 v[90:93], v[172:175], v[234:237], v[90:93]
	v_mfma_f32_16x16x32_bf16 v[78:81], v[164:167], v[242:245], v[78:81]
	v_mfma_f32_16x16x32_bf16 v[74:77], v[172:175], v[242:245], v[74:77]
	s_setprio 0
	s_setprio 1
	v_mfma_f32_16x16x32_bf16 v[118:121], v[176:179], v[192:195], v[118:121]
	v_mfma_f32_16x16x32_bf16 v[114:117], v[184:187], v[192:195], v[114:117]
	v_mfma_f32_16x16x32_bf16 v[102:105], v[176:179], v[200:203], v[102:105]
	v_mfma_f32_16x16x32_bf16 v[98:101], v[184:187], v[200:203], v[98:101]
	v_mfma_f32_16x16x32_bf16 v[86:89], v[176:179], v[230:233], v[86:89]
	v_mfma_f32_16x16x32_bf16 v[82:85], v[184:187], v[230:233], v[82:85]
	v_mfma_f32_16x16x32_bf16 v[70:73], v[176:179], v[238:241], v[70:73]
	v_mfma_f32_16x16x32_bf16 v[66:69], v[184:187], v[238:241], v[66:69]
	v_mfma_f32_16x16x32_bf16 v[118:121], v[180:183], v[196:199], v[118:121]
	v_mfma_f32_16x16x32_bf16 v[114:117], v[188:191], v[196:199], v[114:117]
	v_mfma_f32_16x16x32_bf16 v[102:105], v[180:183], v[204:207], v[102:105]
	v_mfma_f32_16x16x32_bf16 v[98:101], v[188:191], v[204:207], v[98:101]
	v_mfma_f32_16x16x32_bf16 v[86:89], v[180:183], v[234:237], v[86:89]
	v_mfma_f32_16x16x32_bf16 v[82:85], v[188:191], v[234:237], v[82:85]
	v_mfma_f32_16x16x32_bf16 v[70:73], v[180:183], v[242:245], v[70:73]
	v_mfma_f32_16x16x32_bf16 v[66:69], v[188:191], v[242:245], v[66:69]
	s_setprio 0
	s_barrier
	s_add_u32 s26, s24, 0x1000
	s_addc_u32 s27, s25, 0
	s_add_i32 s45, s45, s31
	s_mov_b32 m0, s45
	ds_read_b128 v[192:195], v155 offset:49152
	ds_read_b128 v[196:199], v155 offset:50176
	ds_read_b128 v[200:203], v155 offset:51200
	ds_read_b128 v[204:207], v155 offset:52224
	ds_read_b128 v[230:233], v155 offset:53248
	ds_read_b128 v[234:237], v155 offset:54272
	ds_read_b128 v[238:241], v155 offset:55296
	ds_read_b128 v[242:245], v155 offset:56320
	global_load_lds_dwordx4 v130, s[26:27]
	s_add_i32 m0, s45, 0x2000
	s_add_u32 s24, s24, 0x41000
	v_lshl_add_u64 v[212:213], s[26:27], 0, v[132:133]
	s_addc_u32 s25, s25, 0
	s_add_i32 s26, s46, s31
	global_load_lds_dwordx4 v[212:213], off
	s_mov_b32 m0, s26
	v_lshl_add_u64 v[210:211], v[210:211], 0, s[50:51]
	global_load_lds_dwordx4 v130, s[24:25]
	s_add_i32 m0, s26, 0x2000
	v_lshl_add_u64 v[208:209], v[208:209], 0, s[50:51]
	global_load_lds_dwordx4 v132, s[24:25]
	s_mov_b32 m0, s39
	s_nop 0
	global_load_lds_dwordx4 v[210:211], off
	s_mov_b32 m0, s40
	s_nop 0
	global_load_lds_dwordx4 v[208:209], off
	s_waitcnt vmcnt(8)
	s_waitcnt lgkmcnt(0)
	s_barrier
	s_setprio 1
	s_waitcnt lgkmcnt(0)
	v_mfma_f32_16x16x32_bf16 v[62:65], v[160:163], v[192:195], v[62:65]
	v_mfma_f32_16x16x32_bf16 v[58:61], v[168:171], v[192:195], v[58:61]
	v_mfma_f32_16x16x32_bf16 v[46:49], v[160:163], v[200:203], v[46:49]
	v_mfma_f32_16x16x32_bf16 v[42:45], v[168:171], v[200:203], v[42:45]
	v_mfma_f32_16x16x32_bf16 v[22:25], v[160:163], v[230:233], v[22:25]
	v_mfma_f32_16x16x32_bf16 v[10:13], v[168:171], v[230:233], v[10:13]
	v_mfma_f32_16x16x32_bf16 v[6:9], v[160:163], v[238:241], v[6:9]
	v_mfma_f32_16x16x32_bf16 v[2:5], v[168:171], v[238:241], v[2:5]
	v_mfma_f32_16x16x32_bf16 v[62:65], v[164:167], v[196:199], v[62:65]
	v_mfma_f32_16x16x32_bf16 v[58:61], v[172:175], v[196:199], v[58:61]
	v_mfma_f32_16x16x32_bf16 v[46:49], v[164:167], v[204:207], v[46:49]
	v_mfma_f32_16x16x32_bf16 v[42:45], v[172:175], v[204:207], v[42:45]
	v_mfma_f32_16x16x32_bf16 v[22:25], v[164:167], v[234:237], v[22:25]
	v_mfma_f32_16x16x32_bf16 v[10:13], v[172:175], v[234:237], v[10:13]
	v_mfma_f32_16x16x32_bf16 v[6:9], v[164:167], v[242:245], v[6:9]
	v_mfma_f32_16x16x32_bf16 v[2:5], v[172:175], v[242:245], v[2:5]
	s_setprio 0
	s_setprio 1
	v_mfma_f32_16x16x32_bf16 v[54:57], v[176:179], v[192:195], v[54:57]
	v_mfma_f32_16x16x32_bf16 v[50:53], v[184:187], v[192:195], v[50:53]
	v_mfma_f32_16x16x32_bf16 v[30:33], v[176:179], v[200:203], v[30:33]
	v_mfma_f32_16x16x32_bf16 v[26:29], v[184:187], v[200:203], v[26:29]
	v_mfma_f32_16x16x32_bf16 v[38:41], v[176:179], v[230:233], v[38:41]
	v_mfma_f32_16x16x32_bf16 v[34:37], v[184:187], v[230:233], v[34:37]
	v_mfma_f32_16x16x32_bf16 v[18:21], v[176:179], v[238:241], v[18:21]
	v_mfma_f32_16x16x32_bf16 v[14:17], v[184:187], v[238:241], v[14:17]
	v_mfma_f32_16x16x32_bf16 v[54:57], v[180:183], v[196:199], v[54:57]
	v_mfma_f32_16x16x32_bf16 v[50:53], v[188:191], v[196:199], v[50:53]
	v_mfma_f32_16x16x32_bf16 v[30:33], v[180:183], v[204:207], v[30:33]
	v_mfma_f32_16x16x32_bf16 v[26:29], v[188:191], v[204:207], v[26:29]
	v_mfma_f32_16x16x32_bf16 v[38:41], v[180:183], v[234:237], v[38:41]
	v_mfma_f32_16x16x32_bf16 v[34:37], v[188:191], v[234:237], v[34:37]
	v_mfma_f32_16x16x32_bf16 v[18:21], v[180:183], v[242:245], v[18:21]
	v_mfma_f32_16x16x32_bf16 v[14:17], v[188:191], v[242:245], v[14:17]
	s_setprio 0
	s_barrier
	s_add_i32 s44, s44, 2
	s_add_u32 s19, s19, 0x2000
	s_addc_u32 s43, s43, 0
	s_add_u32 s22, s22, 0x100
	s_addc_u32 s23, s23, 0
	s_cmp_gt_u32 s44, 13
	s_cbranch_scc0 .LBB0_1737
	s_and_b64 vcc, exec, s[16:17]
	s_cbranch_vccz .LBB0_1740
	s_barrier

.LBB0_1839:
	s_add_u32 s16, s14, 0x2000
	s_addc_u32 s17, s15, 0
	s_cmp_eq_u32 s45, 40
	s_cselect_b32 s22, s4, s16
	s_cselect_b32 s23, s5, s17
	s_cselect_b32 s20, s12, s43
	s_cselect_b32 s21, s13, s44
	s_add_u32 s18, s22, 0x1000
	s_addc_u32 s19, s23, 0
	s_add_i32 s46, 0, 0x10000
	v_add_u32_e32 v0, s46, v146
	s_add_i32 s47, 0, 0x14000
	ds_read_b128 v[150:153], v0
	ds_read_b128 v[154:157], v0 offset:1024
	ds_read_b128 v[158:161], v0 offset:2048
	ds_read_b128 v[162:165], v0 offset:3072
	v_add_u32_e32 v0, s47, v146
	ds_read_b128 v[166:169], v0
	ds_read_b128 v[170:173], v0 offset:1024
	ds_read_b128 v[174:177], v0 offset:2048
	ds_read_b128 v[178:181], v0 offset:3072
	s_add_i32 m0, s31, 0xc000
	ds_read_b128 v[182:185], v148
	ds_read_b128 v[186:189], v148 offset:1024
	ds_read_b128 v[190:193], v148 offset:2048
	ds_read_b128 v[194:197], v148 offset:3072
	ds_read_b128 v[198:201], v148 offset:4096
	ds_read_b128 v[202:205], v148 offset:5120
	ds_read_b128 v[206:209], v148 offset:6144
	ds_read_b128 v[230:233], v148 offset:7168
	global_load_lds_dwordx4 v138, s[14:15]
	s_add_i32 m0, s31, 0xe000
	s_nop 0
	global_load_lds_dwordx4 v140, s[14:15]
	s_waitcnt vmcnt(8)
	s_waitcnt lgkmcnt(0)
	s_barrier
	s_setprio 1
	s_waitcnt lgkmcnt(0)
	v_mfma_f32_16x16x32_bf16 v[126:129], v[150:153], v[182:185], v[126:129]
	v_mfma_f32_16x16x32_bf16 v[122:125], v[158:161], v[182:185], v[122:125]
	v_mfma_f32_16x16x32_bf16 v[118:121], v[150:153], v[190:193], v[118:121]
	v_mfma_f32_16x16x32_bf16 v[110:113], v[158:161], v[190:193], v[110:113]
	v_mfma_f32_16x16x32_bf16 v[102:105], v[150:153], v[198:201], v[102:105]
	v_mfma_f32_16x16x32_bf16 v[94:97], v[158:161], v[198:201], v[94:97]
	v_mfma_f32_16x16x32_bf16 v[86:89], v[150:153], v[206:209], v[86:89]
	v_mfma_f32_16x16x32_bf16 v[78:81], v[158:161], v[206:209], v[78:81]
	v_mfma_f32_16x16x32_bf16 v[126:129], v[154:157], v[186:189], v[126:129]
	v_mfma_f32_16x16x32_bf16 v[122:125], v[162:165], v[186:189], v[122:125]
	v_mfma_f32_16x16x32_bf16 v[118:121], v[154:157], v[194:197], v[118:121]
	v_mfma_f32_16x16x32_bf16 v[110:113], v[162:165], v[194:197], v[110:113]
	v_mfma_f32_16x16x32_bf16 v[102:105], v[154:157], v[202:205], v[102:105]
	v_mfma_f32_16x16x32_bf16 v[94:97], v[162:165], v[202:205], v[94:97]
	v_mfma_f32_16x16x32_bf16 v[86:89], v[154:157], v[230:233], v[86:89]
	v_mfma_f32_16x16x32_bf16 v[78:81], v[162:165], v[230:233], v[78:81]
	s_setprio 0
	s_setprio 1
	v_mfma_f32_16x16x32_bf16 v[114:117], v[166:169], v[182:185], v[114:117]
	v_mfma_f32_16x16x32_bf16 v[106:109], v[174:177], v[182:185], v[106:109]
	v_mfma_f32_16x16x32_bf16 v[98:101], v[166:169], v[190:193], v[98:101]
	v_mfma_f32_16x16x32_bf16 v[90:93], v[174:177], v[190:193], v[90:93]
	v_mfma_f32_16x16x32_bf16 v[82:85], v[166:169], v[198:201], v[82:85]
	v_mfma_f32_16x16x32_bf16 v[74:77], v[174:177], v[198:201], v[74:77]
	v_mfma_f32_16x16x32_bf16 v[62:65], v[166:169], v[206:209], v[62:65]
	v_mfma_f32_16x16x32_bf16 v[58:61], v[174:177], v[206:209], v[58:61]
	v_mfma_f32_16x16x32_bf16 v[114:117], v[170:173], v[186:189], v[114:117]
	v_mfma_f32_16x16x32_bf16 v[106:109], v[178:181], v[186:189], v[106:109]
	v_mfma_f32_16x16x32_bf16 v[98:101], v[170:173], v[194:197], v[98:101]
	v_mfma_f32_16x16x32_bf16 v[90:93], v[178:181], v[194:197], v[90:93]
	v_mfma_f32_16x16x32_bf16 v[82:85], v[170:173], v[202:205], v[82:85]
	v_mfma_f32_16x16x32_bf16 v[74:77], v[178:181], v[202:205], v[74:77]
	v_mfma_f32_16x16x32_bf16 v[62:65], v[170:173], v[230:233], v[62:65]
	v_mfma_f32_16x16x32_bf16 v[58:61], v[178:181], v[230:233], v[58:61]
	s_setprio 0
	s_barrier
	s_add_i32 s14, s46, s30
	s_mov_b32 m0, s14
	ds_read_b128 v[182:185], v148 offset:16384
	ds_read_b128 v[186:189], v148 offset:17408
	ds_read_b128 v[190:193], v148 offset:18432
	ds_read_b128 v[194:197], v148 offset:19456
	ds_read_b128 v[198:201], v148 offset:20480
	ds_read_b128 v[202:205], v148 offset:21504
	ds_read_b128 v[206:209], v148 offset:22528
	ds_read_b128 v[230:233], v148 offset:23552
	global_load_lds_dwordx4 v134, s[20:21]
	s_add_i32 m0, s14, 0x2000
	s_add_u32 s14, s20, 0xb0000
	s_addc_u32 s15, s21, 0
	s_add_i32 s46, s47, s30
	global_load_lds_dwordx4 v130, s[20:21]
	s_mov_b32 m0, s46
	s_nop 0
	global_load_lds_dwordx4 v134, s[14:15]
	s_add_i32 m0, s46, 0x2000
	s_nop 0
	global_load_lds_dwordx4 v130, s[14:15]
	s_mov_b32 m0, s31
	s_nop 0
	global_load_lds_dwordx4 v136, s[22:23]
	s_mov_b32 m0, s33
	s_nop 0
	global_load_lds_dwordx4 v132, s[22:23]
	s_waitcnt vmcnt(8)
	s_waitcnt lgkmcnt(0)
	s_barrier
	s_setprio 1
	s_waitcnt lgkmcnt(0)
	v_mfma_f32_16x16x32_bf16 v[46:49], v[150:153], v[182:185], v[46:49]
	v_mfma_f32_16x16x32_bf16 v[42:45], v[158:161], v[182:185], v[42:45]
	v_mfma_f32_16x16x32_bf16 v[30:33], v[150:153], v[190:193], v[30:33]
	v_mfma_f32_16x16x32_bf16 v[18:21], v[158:161], v[190:193], v[18:21]
	v_mfma_f32_16x16x32_bf16 v[14:17], v[150:153], v[198:201], v[14:17]
	v_mfma_f32_16x16x32_bf16 v[10:13], v[158:161], v[198:201], v[10:13]
	v_mfma_f32_16x16x32_bf16 v[6:9], v[150:153], v[206:209], v[6:9]
	v_mfma_f32_16x16x32_bf16 v[2:5], v[158:161], v[206:209], v[2:5]
	v_mfma_f32_16x16x32_bf16 v[46:49], v[154:157], v[186:189], v[46:49]
	v_mfma_f32_16x16x32_bf16 v[42:45], v[162:165], v[186:189], v[42:45]
	v_mfma_f32_16x16x32_bf16 v[30:33], v[154:157], v[194:197], v[30:33]
	v_mfma_f32_16x16x32_bf16 v[18:21], v[162:165], v[194:197], v[18:21]
	v_mfma_f32_16x16x32_bf16 v[14:17], v[154:157], v[202:205], v[14:17]
	v_mfma_f32_16x16x32_bf16 v[10:13], v[162:165], v[202:205], v[10:13]
	v_mfma_f32_16x16x32_bf16 v[6:9], v[154:157], v[230:233], v[6:9]
	v_mfma_f32_16x16x32_bf16 v[2:5], v[162:165], v[230:233], v[2:5]
	s_setprio 0
	s_setprio 1
	v_mfma_f32_16x16x32_bf16 v[66:69], v[166:169], v[182:185], v[66:69]
	v_mfma_f32_16x16x32_bf16 v[70:73], v[174:177], v[182:185], v[70:73]
	v_mfma_f32_16x16x32_bf16 v[50:53], v[166:169], v[190:193], v[50:53]
	v_mfma_f32_16x16x32_bf16 v[54:57], v[174:177], v[190:193], v[54:57]
	v_mfma_f32_16x16x32_bf16 v[34:37], v[166:169], v[198:201], v[34:37]
	v_mfma_f32_16x16x32_bf16 v[38:41], v[174:177], v[198:201], v[38:41]
	v_mfma_f32_16x16x32_bf16 v[22:25], v[166:169], v[206:209], v[22:25]
	v_mfma_f32_16x16x32_bf16 v[26:29], v[174:177], v[206:209], v[26:29]
	v_mfma_f32_16x16x32_bf16 v[66:69], v[170:173], v[186:189], v[66:69]
	v_mfma_f32_16x16x32_bf16 v[70:73], v[178:181], v[186:189], v[70:73]
	v_mfma_f32_16x16x32_bf16 v[50:53], v[170:173], v[194:197], v[50:53]
	v_mfma_f32_16x16x32_bf16 v[54:57], v[178:181], v[194:197], v[54:57]
	v_mfma_f32_16x16x32_bf16 v[34:37], v[170:173], v[202:205], v[34:37]
	v_mfma_f32_16x16x32_bf16 v[38:41], v[178:181], v[202:205], v[38:41]
	v_mfma_f32_16x16x32_bf16 v[22:25], v[170:173], v[230:233], v[22:25]
	v_mfma_f32_16x16x32_bf16 v[26:29], v[178:181], v[230:233], v[26:29]
	s_setprio 0
	s_barrier
	s_add_i32 s46, 0, 0x18000
	v_add_u32_e32 v0, s46, v146
	s_add_i32 s47, 0, 0x1c000
	ds_read_b128 v[150:153], v0
	ds_read_b128 v[154:157], v0 offset:1024
	ds_read_b128 v[158:161], v0 offset:2048
	ds_read_b128 v[162:165], v0 offset:3072
	v_add_u32_e32 v0, s47, v146
	ds_read_b128 v[166:169], v0
	ds_read_b128 v[170:173], v0 offset:1024
	ds_read_b128 v[174:177], v0 offset:2048
	ds_read_b128 v[178:181], v0 offset:3072
	s_add_u32 s14, s22, 0xb0000
	s_addc_u32 s15, s23, 0
	s_mov_b32 m0, s34
	ds_read_b128 v[182:185], v148 offset:32768
	ds_read_b128 v[186:189], v148 offset:33792
	ds_read_b128 v[190:193], v148 offset:34816
	ds_read_b128 v[194:197], v148 offset:35840
	ds_read_b128 v[198:201], v148 offset:36864
	ds_read_b128 v[202:205], v148 offset:37888
	ds_read_b128 v[206:209], v148 offset:38912
	ds_read_b128 v[230:233], v148 offset:39936
	global_load_lds_dwordx4 v136, s[14:15]
	s_mov_b32 m0, s35
	s_nop 0
	global_load_lds_dwordx4 v132, s[14:15]
	s_waitcnt vmcnt(8)
	s_waitcnt lgkmcnt(0)
	s_barrier
	s_setprio 1
	s_waitcnt lgkmcnt(0)
	v_mfma_f32_16x16x32_bf16 v[126:129], v[150:153], v[182:185], v[126:129]
	v_mfma_f32_16x16x32_bf16 v[122:125], v[158:161], v[182:185], v[122:125]
	v_mfma_f32_16x16x32_bf16 v[118:121], v[150:153], v[190:193], v[118:121]
	v_mfma_f32_16x16x32_bf16 v[110:113], v[158:161], v[190:193], v[110:113]
	v_mfma_f32_16x16x32_bf16 v[102:105], v[150:153], v[198:201], v[102:105]
	v_mfma_f32_16x16x32_bf16 v[94:97], v[158:161], v[198:201], v[94:97]
	v_mfma_f32_16x16x32_bf16 v[86:89], v[150:153], v[206:209], v[86:89]
	v_mfma_f32_16x16x32_bf16 v[78:81], v[158:161], v[206:209], v[78:81]
	v_mfma_f32_16x16x32_bf16 v[126:129], v[154:157], v[186:189], v[126:129]
	v_mfma_f32_16x16x32_bf16 v[122:125], v[162:165], v[186:189], v[122:125]
	v_mfma_f32_16x16x32_bf16 v[118:121], v[154:157], v[194:197], v[118:121]
	v_mfma_f32_16x16x32_bf16 v[110:113], v[162:165], v[194:197], v[110:113]
	v_mfma_f32_16x16x32_bf16 v[102:105], v[154:157], v[202:205], v[102:105]
	v_mfma_f32_16x16x32_bf16 v[94:97], v[162:165], v[202:205], v[94:97]
	v_mfma_f32_16x16x32_bf16 v[86:89], v[154:157], v[230:233], v[86:89]
	v_mfma_f32_16x16x32_bf16 v[78:81], v[162:165], v[230:233], v[78:81]
	s_setprio 0
	s_setprio 1
	v_mfma_f32_16x16x32_bf16 v[114:117], v[166:169], v[182:185], v[114:117]
	v_mfma_f32_16x16x32_bf16 v[106:109], v[174:177], v[182:185], v[106:109]
	v_mfma_f32_16x16x32_bf16 v[98:101], v[166:169], v[190:193], v[98:101]
	v_mfma_f32_16x16x32_bf16 v[90:93], v[174:177], v[190:193], v[90:93]
	v_mfma_f32_16x16x32_bf16 v[82:85], v[166:169], v[198:201], v[82:85]
	v_mfma_f32_16x16x32_bf16 v[74:77], v[174:177], v[198:201], v[74:77]
	v_mfma_f32_16x16x32_bf16 v[62:65], v[166:169], v[206:209], v[62:65]
	v_mfma_f32_16x16x32_bf16 v[58:61], v[174:177], v[206:209], v[58:61]
	v_mfma_f32_16x16x32_bf16 v[114:117], v[170:173], v[186:189], v[114:117]
	v_mfma_f32_16x16x32_bf16 v[106:109], v[178:181], v[186:189], v[106:109]
	v_mfma_f32_16x16x32_bf16 v[98:101], v[170:173], v[194:197], v[98:101]
	v_mfma_f32_16x16x32_bf16 v[90:93], v[178:181], v[194:197], v[90:93]
	v_mfma_f32_16x16x32_bf16 v[82:85], v[170:173], v[202:205], v[82:85]
	v_mfma_f32_16x16x32_bf16 v[74:77], v[178:181], v[202:205], v[74:77]
	v_mfma_f32_16x16x32_bf16 v[62:65], v[170:173], v[230:233], v[62:65]
	v_mfma_f32_16x16x32_bf16 v[58:61], v[178:181], v[230:233], v[58:61]
	s_setprio 0
	s_barrier
	s_add_u32 s14, s20, 0x1000
	s_addc_u32 s15, s21, 0
	s_add_i32 s22, s46, s30
	s_mov_b32 m0, s22
	ds_read_b128 v[182:185], v148 offset:49152
	ds_read_b128 v[186:189], v148 offset:50176
	ds_read_b128 v[190:193], v148 offset:51200
	ds_read_b128 v[194:197], v148 offset:52224
	ds_read_b128 v[198:201], v148 offset:53248
	ds_read_b128 v[202:205], v148 offset:54272
	ds_read_b128 v[206:209], v148 offset:55296
	ds_read_b128 v[230:233], v148 offset:56320
	global_load_lds_dwordx4 v134, s[14:15]
	s_add_i32 m0, s22, 0x2000
	v_lshl_add_u64 v[210:211], s[14:15], 0, v[130:131]
	s_add_u32 s14, s20, 0xb1000
	s_addc_u32 s15, s21, 0
	s_add_i32 s20, s47, s30
	global_load_lds_dwordx4 v[210:211], off
	s_mov_b32 m0, s20
	s_nop 0
	global_load_lds_dwordx4 v134, s[14:15]
	s_add_i32 m0, s20, 0x2000
	s_nop 0
	global_load_lds_dwordx4 v130, s[14:15]
	s_mov_b32 m0, s36
	s_nop 0
	global_load_lds_dwordx4 v136, s[18:19]
	s_mov_b32 m0, s37
	s_nop 0
	global_load_lds_dwordx4 v132, s[18:19]
	s_waitcnt vmcnt(8)
	s_waitcnt lgkmcnt(0)
	s_barrier
	s_setprio 1
	s_waitcnt lgkmcnt(0)
	v_mfma_f32_16x16x32_bf16 v[46:49], v[150:153], v[182:185], v[46:49]
	v_mfma_f32_16x16x32_bf16 v[42:45], v[158:161], v[182:185], v[42:45]
	v_mfma_f32_16x16x32_bf16 v[30:33], v[150:153], v[190:193], v[30:33]
	v_mfma_f32_16x16x32_bf16 v[18:21], v[158:161], v[190:193], v[18:21]
	v_mfma_f32_16x16x32_bf16 v[14:17], v[150:153], v[198:201], v[14:17]
	v_mfma_f32_16x16x32_bf16 v[10:13], v[158:161], v[198:201], v[10:13]
	v_mfma_f32_16x16x32_bf16 v[6:9], v[150:153], v[206:209], v[6:9]
	v_mfma_f32_16x16x32_bf16 v[2:5], v[158:161], v[206:209], v[2:5]
	v_mfma_f32_16x16x32_bf16 v[46:49], v[154:157], v[186:189], v[46:49]
	v_mfma_f32_16x16x32_bf16 v[42:45], v[162:165], v[186:189], v[42:45]
	v_mfma_f32_16x16x32_bf16 v[30:33], v[154:157], v[194:197], v[30:33]
	v_mfma_f32_16x16x32_bf16 v[18:21], v[162:165], v[194:197], v[18:21]
	v_mfma_f32_16x16x32_bf16 v[14:17], v[154:157], v[202:205], v[14:17]
	v_mfma_f32_16x16x32_bf16 v[10:13], v[162:165], v[202:205], v[10:13]
	v_mfma_f32_16x16x32_bf16 v[6:9], v[154:157], v[230:233], v[6:9]
	v_mfma_f32_16x16x32_bf16 v[2:5], v[162:165], v[230:233], v[2:5]
	s_setprio 0
	s_setprio 1
	v_mfma_f32_16x16x32_bf16 v[66:69], v[166:169], v[182:185], v[66:69]
	v_mfma_f32_16x16x32_bf16 v[70:73], v[174:177], v[182:185], v[70:73]
	v_mfma_f32_16x16x32_bf16 v[50:53], v[166:169], v[190:193], v[50:53]
	v_mfma_f32_16x16x32_bf16 v[54:57], v[174:177], v[190:193], v[54:57]
	v_mfma_f32_16x16x32_bf16 v[34:37], v[166:169], v[198:201], v[34:37]
	v_mfma_f32_16x16x32_bf16 v[38:41], v[174:177], v[198:201], v[38:41]
	v_mfma_f32_16x16x32_bf16 v[22:25], v[166:169], v[206:209], v[22:25]
	v_mfma_f32_16x16x32_bf16 v[26:29], v[174:177], v[206:209], v[26:29]
	v_mfma_f32_16x16x32_bf16 v[66:69], v[170:173], v[186:189], v[66:69]
	v_mfma_f32_16x16x32_bf16 v[70:73], v[178:181], v[186:189], v[70:73]
	v_mfma_f32_16x16x32_bf16 v[50:53], v[170:173], v[194:197], v[50:53]
	v_mfma_f32_16x16x32_bf16 v[54:57], v[178:181], v[194:197], v[54:57]
	v_mfma_f32_16x16x32_bf16 v[34:37], v[170:173], v[202:205], v[34:37]
	v_mfma_f32_16x16x32_bf16 v[38:41], v[178:181], v[202:205], v[38:41]
	v_mfma_f32_16x16x32_bf16 v[22:25], v[170:173], v[230:233], v[22:25]
	v_mfma_f32_16x16x32_bf16 v[26:29], v[178:181], v[230:233], v[26:29]
	s_setprio 0
	s_barrier
	s_add_i32 s45, s45, 2
	s_add_u32 s43, s43, 0x2000
	s_addc_u32 s44, s44, 0
	s_cmp_gt_u32 s45, 41
	s_mov_b64 s[14:15], s[16:17]
	s_cbranch_scc0 .LBB0_1839
	s_and_b64 vcc, exec, s[10:11]
	s_cbranch_vccz .LBB0_1842
	s_barrier
